# outproj blockIdx remapped so the four column tiles of an A row-tile share an XCD L2; qkv BK=64 K loop; fixup V path
# baseline (speedup 1.0000x reference)
_Z9k_outprojPKDF16_S0_PKfPf:
	s_load_dwordx8 s[4:11], s[0:1], 0x0
	s_and_b32 s12, s2, 7
	s_lshr_b32 s13, s2, 3
	s_mul_i32 s14, s12, 43
	s_min_u32 s12, s12, 4
	s_add_u32 s14, s14, s12
	s_add_u32 s2, s14, s13
	v_and_b32_e32 v3, 31, v0
	s_and_b32 s1, s2, 3
	v_lshlrev_b32_e32 v1, 2, v3
	v_lshl_or_b32 v66, s1, 9, v1
	s_waitcnt lgkmcnt(0)
	global_load_dword v50, v66, s[8:9]
	global_load_dword v34, v66, s[8:9] offset:128
	global_load_dword v18, v66, s[8:9] offset:256
	v_lshrrev_b32_e32 v4, 6, v0
	v_bfe_u32 v1, v0, 3, 3
	s_lshl_b32 s0, s2, 5
	v_lshl_or_b32 v2, v4, 3, v1
	s_and_b32 s0, s0, 0x7fffff80
	v_lshrrev_b32_e32 v5, 1, v2
	v_or_b32_e32 v7, s0, v2
	v_lshlrev_b32_e32 v8, 9, v2
	v_or_b32_e32 v9, 32, v2
	v_or_b32_e32 v10, 64, v2
	v_or_b32_e32 v2, 0x60, v2
	v_xor_b32_e32 v5, v5, v0
	v_or_b32_e32 v14, s0, v2
	v_lshlrev_b32_e32 v15, 9, v2
	v_lshlrev_b32_e32 v2, 3, v5
	v_and_b32_e32 v5, 56, v2
	global_load_dword v2, v66, s[8:9] offset:384
	v_lshlrev_b32_e32 v1, 5, v4
	v_or_b32_e32 v11, v1, v3
	v_lshlrev_b32_e32 v104, 7, v11
	v_lshlrev_b32_e32 v11, 10, v4
	v_mov_b32_e32 v67, 0
	s_lshl_b32 s1, s1, 16
	v_min_u32_e32 v7, 0x2b17, v7
	v_or_b32_e32 v12, s0, v9
	v_lshlrev_b32_e32 v9, 9, v9
	v_or_b32_e32 v13, s0, v10
	v_lshlrev_b32_e32 v10, 9, v10
	v_lshlrev_b32_e32 v16, 1, v5
	v_readfirstlane_b32 s9, v11
	v_or3_b32 v8, v8, s1, v5
	v_or3_b32 v9, v9, s1, v5
	v_or3_b32 v10, v10, s1, v5
	v_or3_b32 v15, v15, s1, v5
	v_lshl_or_b32 v4, v7, 10, v16
	v_mov_b32_e32 v5, v67
	s_mov_b32 m0, s9
	v_lshl_add_u64 v[68:69], s[4:5], 0, v[4:5]
	global_load_lds_dwordx4 v4, s[4:5]
	v_lshlrev_b32_e32 v4, 1, v8
	v_min_u32_e32 v12, 0x2b17, v12
	v_lshl_add_u64 v[70:71], s[6:7], 0, v[4:5]
	v_or_b32_e32 v4, 0x4000, v11
	v_min_u32_e32 v13, 0x2b17, v13
	v_readfirstlane_b32 s12, v4
	v_lshl_or_b32 v4, v12, 10, v16
	v_lshl_add_u64 v[72:73], s[4:5], 0, v[4:5]
	v_or_b32_e32 v5, 0x1000, v11
	s_mov_b32 m0, s12
	v_readfirstlane_b32 s13, v5
	global_load_lds_dwordx4 v[70:71], off
	s_mov_b32 m0, s13
	v_mov_b32_e32 v5, v67
	global_load_lds_dwordx4 v4, s[4:5]
	v_lshlrev_b32_e32 v4, 1, v9
	v_lshl_add_u64 v[74:75], s[6:7], 0, v[4:5]
	v_or_b32_e32 v4, 0x5000, v11
	v_min_u32_e32 v14, 0x2b17, v14
	v_readfirstlane_b32 s14, v4
	v_lshl_or_b32 v4, v13, 10, v16
	v_lshl_add_u64 v[76:77], s[4:5], 0, v[4:5]
	v_or_b32_e32 v5, 0x2000, v11
	s_mov_b32 m0, s14
	v_readfirstlane_b32 s15, v5
	global_load_lds_dwordx4 v[74:75], off
	s_mov_b32 m0, s15
	v_mov_b32_e32 v5, v67
	global_load_lds_dwordx4 v4, s[4:5]
	v_lshlrev_b32_e32 v4, 1, v10
	v_lshl_add_u64 v[78:79], s[6:7], 0, v[4:5]
	v_or_b32_e32 v4, 0x6000, v11
	v_or_b32_e32 v7, 0x8000, v11
	v_readfirstlane_b32 s16, v4
	v_lshl_or_b32 v4, v14, 10, v16
	v_lshl_add_u64 v[80:81], s[4:5], 0, v[4:5]
	v_or_b32_e32 v5, 0x3000, v11
	s_mov_b32 m0, s16
	v_readfirstlane_b32 s17, v5
	global_load_lds_dwordx4 v[78:79], off
	s_mov_b32 m0, s17
	v_mov_b32_e32 v5, v67
	global_load_lds_dwordx4 v4, s[4:5]
	v_lshlrev_b32_e32 v4, 1, v15
	v_lshl_add_u64 v[82:83], s[6:7], 0, v[4:5]
	v_or_b32_e32 v4, 0x7000, v11
	s_mov_b64 s[20:21], 0x80
	v_readfirstlane_b32 s18, v4
	s_mov_b32 m0, s18
	v_readfirstlane_b32 s1, v7
	v_or_b32_e32 v7, 0xc000, v11
	global_load_lds_dwordx4 v[82:83], off
	v_lshl_add_u64 v[4:5], v[68:69], 0, s[20:21]
	s_mov_b32 m0, s1
	v_readfirstlane_b32 s2, v7
	v_or_b32_e32 v7, 0x9000, v11
	s_waitcnt vmcnt(0) lgkmcnt(0)
	s_barrier
	global_load_lds_dwordx4 v[4:5], off
	v_lshl_add_u64 v[4:5], v[70:71], 0, s[20:21]
	s_mov_b32 m0, s2
	v_readfirstlane_b32 s3, v7
	v_or_b32_e32 v7, 0xd000, v11
	global_load_lds_dwordx4 v[4:5], off
	v_lshl_add_u64 v[4:5], v[72:73], 0, s[20:21]
	s_mov_b32 m0, s3
	v_readfirstlane_b32 s4, v7
	v_or_b32_e32 v7, 0xa000, v11
	global_load_lds_dwordx4 v[4:5], off
	v_lshl_add_u64 v[4:5], v[74:75], 0, s[20:21]
	s_mov_b32 m0, s4
	v_readfirstlane_b32 s5, v7
	v_or_b32_e32 v7, 0xe000, v11
	global_load_lds_dwordx4 v[4:5], off
	v_lshl_add_u64 v[4:5], v[76:77], 0, s[20:21]
	s_mov_b32 m0, s5
	v_readfirstlane_b32 s6, v7
	v_or_b32_e32 v7, 0xb000, v11
	global_load_lds_dwordx4 v[4:5], off
	v_lshl_add_u64 v[4:5], v[78:79], 0, s[20:21]
	s_mov_b32 m0, s6
	v_readfirstlane_b32 s7, v7
	v_or_b32_e32 v7, 0xf000, v11
	global_load_lds_dwordx4 v[4:5], off
	v_lshl_add_u64 v[4:5], v[80:81], 0, s[20:21]
	s_mov_b32 m0, s7
	v_readfirstlane_b32 s8, v7
	v_lshrrev_b32_e32 v6, 1, v0
	v_bfe_u32 v84, v0, 5, 1
	global_load_lds_dwordx4 v[4:5], off
	v_lshl_add_u64 v[4:5], v[82:83], 0, s[20:21]
	s_mov_b32 m0, s8
	v_lshlrev_b32_e32 v105, 7, v3
	global_load_lds_dwordx4 v[4:5], off
	v_bitop3_b32 v4, v84, v6, 7 bitop3:0x78
	v_lshlrev_b32_e32 v4, 4, v4
	v_or_b32_e32 v86, v104, v4
	ds_read_b128 v[90:93], v86
	v_or_b32_e32 v85, v105, v4
	ds_read_b128 v[94:97], v85 offset:24576
	ds_read_b128 v[6:9], v85 offset:16384
	ds_read_b128 v[10:13], v85 offset:20480
	v_bfe_u32 v106, v0, 1, 3
	v_bitop3_b32 v0, v84, v106, 2 bitop3:0x36
	v_mov_b32_e32 v19, v18
	v_mov_b32_e32 v20, v18
	v_mov_b32_e32 v21, v18
	v_mov_b32_e32 v22, v18
	v_mov_b32_e32 v23, v18
	v_mov_b32_e32 v24, v18
	v_mov_b32_e32 v25, v18
	v_mov_b32_e32 v26, v18
	v_mov_b32_e32 v27, v18
	v_mov_b32_e32 v28, v18
	v_mov_b32_e32 v29, v18
	v_mov_b32_e32 v30, v18
	v_mov_b32_e32 v31, v18
	v_mov_b32_e32 v32, v18
	v_mov_b32_e32 v33, v18
	v_lshlrev_b32_e32 v0, 4, v0
	v_or_b32_e32 v88, v104, v0
	s_waitcnt lgkmcnt(0)
	v_mfma_f32_32x32x16_f16 v[18:33], v[90:93], v[94:97], v[18:33]
	ds_read_b128 v[94:97], v85 offset:28672
	ds_read_b128 v[98:101], v88
	v_mov_b32_e32 v51, v50
	v_mov_b32_e32 v52, v50
	v_mov_b32_e32 v53, v50
	v_mov_b32_e32 v54, v50
	v_mov_b32_e32 v55, v50
	v_mov_b32_e32 v56, v50
	v_mov_b32_e32 v57, v50
	v_mov_b32_e32 v58, v50
	v_mov_b32_e32 v59, v50
	v_mov_b32_e32 v60, v50
	v_mov_b32_e32 v61, v50
	v_mov_b32_e32 v62, v50
	v_mov_b32_e32 v63, v50
	v_mov_b32_e32 v64, v50
	v_mov_b32_e32 v65, v50
	v_mov_b32_e32 v35, v34
	v_mov_b32_e32 v36, v34
	v_mov_b32_e32 v37, v34
	v_mov_b32_e32 v38, v34
	v_mov_b32_e32 v39, v34
	v_mov_b32_e32 v40, v34
	v_mov_b32_e32 v41, v34
	v_mov_b32_e32 v42, v34
	v_mov_b32_e32 v43, v34
	v_mov_b32_e32 v44, v34
	v_mov_b32_e32 v45, v34
	v_mov_b32_e32 v46, v34
	v_mov_b32_e32 v47, v34
	v_mov_b32_e32 v48, v34
	v_mov_b32_e32 v49, v34
	v_mfma_f32_32x32x16_f16 v[50:65], v[90:93], v[6:9], v[50:65]
	v_mov_b32_e32 v3, v2
	v_mov_b32_e32 v4, v2
	v_mov_b32_e32 v5, v2
	v_mov_b32_e32 v6, v2
	v_mov_b32_e32 v7, v2
	v_mov_b32_e32 v8, v2
	v_mov_b32_e32 v9, v2
	v_mfma_f32_32x32x16_f16 v[34:49], v[90:93], v[10:13], v[34:49]
	v_mov_b32_e32 v10, v2
	v_mov_b32_e32 v11, v2
	v_mov_b32_e32 v12, v2
	v_mov_b32_e32 v13, v2
	v_mov_b32_e32 v14, v2
	v_mov_b32_e32 v15, v2
	v_mov_b32_e32 v16, v2
	v_mov_b32_e32 v17, v2
	v_or_b32_e32 v0, v105, v0
	v_bitop3_b32 v87, v84, v106, 4 bitop3:0x36
	s_waitcnt lgkmcnt(0)
	v_mfma_f32_32x32x16_f16 v[2:17], v[90:93], v[94:97], v[2:17]
	ds_read_b128 v[90:93], v0 offset:16384
	ds_read_b128 v[94:97], v0 offset:20480
	v_lshlrev_b32_e32 v87, 4, v87
	v_or_b32_e32 v89, v104, v87
	v_or_b32_e32 v87, v105, v87
	s_mov_b64 s[20:21], 0x100
	s_mov_b32 m0, s9
	s_cmpk_gt_u32 s0, 0x2a98
	s_waitcnt lgkmcnt(0)
	v_mfma_f32_32x32x16_f16 v[50:65], v[98:101], v[90:93], v[50:65]
	v_mfma_f32_32x32x16_f16 v[34:49], v[98:101], v[94:97], v[34:49]
	ds_read_b128 v[90:93], v0 offset:24576
	ds_read_b128 v[94:97], v0 offset:28672
	s_waitcnt lgkmcnt(0)
	v_mfma_f32_32x32x16_f16 v[18:33], v[98:101], v[90:93], v[18:33]
	v_bitop3_b32 v90, v84, v106, 6 bitop3:0x36
	v_lshlrev_b32_e32 v90, 4, v90
	v_or_b32_e32 v91, v104, v90
	v_or_b32_e32 v90, v105, v90
	v_mfma_f32_32x32x16_f16 v[2:17], v[98:101], v[94:97], v[2:17]
	ds_read_b128 v[92:95], v89
	ds_read_b128 v[96:99], v87 offset:16384
	s_waitcnt lgkmcnt(0)
	v_mfma_f32_32x32x16_f16 v[50:65], v[92:95], v[96:99], v[50:65]
	ds_read_b128 v[96:99], v87 offset:20480
	ds_read_b128 v[100:103], v87 offset:24576
	s_waitcnt lgkmcnt(0)
	v_mfma_f32_32x32x16_f16 v[34:49], v[92:95], v[96:99], v[34:49]
	ds_read_b128 v[96:99], v87 offset:28672
	v_mfma_f32_32x32x16_f16 v[18:33], v[92:95], v[100:103], v[18:33]
	ds_read_b128 v[100:103], v91
	s_waitcnt lgkmcnt(0)
	v_mfma_f32_32x32x16_f16 v[2:17], v[92:95], v[96:99], v[2:17]
	ds_read_b128 v[92:95], v90 offset:16384
	ds_read_b128 v[96:99], v90 offset:20480
	s_waitcnt lgkmcnt(0)
	v_mfma_f32_32x32x16_f16 v[50:65], v[100:103], v[92:95], v[50:65]
	v_mfma_f32_32x32x16_f16 v[34:49], v[100:103], v[96:99], v[34:49]
	ds_read_b128 v[92:95], v90 offset:24576
	ds_read_b128 v[96:99], v90 offset:28672
	s_waitcnt vmcnt(0) lgkmcnt(0)
	s_barrier
	v_mfma_f32_32x32x16_f16 v[18:33], v[100:103], v[92:95], v[18:33]
	v_lshl_add_u64 v[92:93], v[68:69], 0, s[20:21]
	global_load_lds_dwordx4 v[92:93], off
	v_lshl_add_u64 v[92:93], v[70:71], 0, s[20:21]
	s_mov_b32 m0, s12
	s_nop 0
	global_load_lds_dwordx4 v[92:93], off
	v_lshl_add_u64 v[92:93], v[72:73], 0, s[20:21]
	s_mov_b32 m0, s13
	v_mfma_f32_32x32x16_f16 v[2:17], v[100:103], v[96:99], v[2:17]
	global_load_lds_dwordx4 v[92:93], off
	v_lshl_add_u64 v[92:93], v[74:75], 0, s[20:21]
	s_mov_b32 m0, s14
	s_nop 0
	global_load_lds_dwordx4 v[92:93], off
	v_lshl_add_u64 v[92:93], v[76:77], 0, s[20:21]
	s_mov_b32 m0, s15
	s_nop 0
	global_load_lds_dwordx4 v[92:93], off
	v_lshl_add_u64 v[92:93], v[78:79], 0, s[20:21]
	s_mov_b32 m0, s16
	s_nop 0
	global_load_lds_dwordx4 v[92:93], off
	v_lshl_add_u64 v[92:93], v[80:81], 0, s[20:21]
	s_mov_b32 m0, s17
	s_nop 0
	global_load_lds_dwordx4 v[92:93], off
	v_lshl_add_u64 v[92:93], v[82:83], 0, s[20:21]
	s_mov_b32 m0, s18
	s_mov_b64 s[20:21], 0x180
	global_load_lds_dwordx4 v[92:93], off
	ds_read_b128 v[92:95], v86 offset:32768
	ds_read_b128 v[96:99], v85 offset:49152
	s_waitcnt lgkmcnt(0)
	v_mfma_f32_32x32x16_f16 v[50:65], v[92:95], v[96:99], v[50:65]
	ds_read_b128 v[96:99], v85 offset:53248
	ds_read_b128 v[100:103], v85 offset:57344
	s_mov_b32 m0, s1
	s_waitcnt lgkmcnt(0)
	v_mfma_f32_32x32x16_f16 v[34:49], v[92:95], v[96:99], v[34:49]
	v_mfma_f32_32x32x16_f16 v[18:33], v[92:95], v[100:103], v[18:33]
	ds_read_b128 v[96:99], v85 offset:61440
	ds_read_b128 v[100:103], v88 offset:32768
	s_waitcnt lgkmcnt(0)
	v_mfma_f32_32x32x16_f16 v[2:17], v[92:95], v[96:99], v[2:17]
	ds_read_b128 v[92:95], v0 offset:49152
	ds_read_b128 v[96:99], v0 offset:53248
	s_waitcnt lgkmcnt(0)
	v_mfma_f32_32x32x16_f16 v[50:65], v[100:103], v[92:95], v[50:65]
	v_mfma_f32_32x32x16_f16 v[34:49], v[100:103], v[96:99], v[34:49]
	ds_read_b128 v[92:95], v0 offset:57344
	ds_read_b128 v[96:99], v0 offset:61440
	s_waitcnt lgkmcnt(0)
	v_mfma_f32_32x32x16_f16 v[18:33], v[100:103], v[92:95], v[18:33]
	v_mfma_f32_32x32x16_f16 v[2:17], v[100:103], v[96:99], v[2:17]
	ds_read_b128 v[92:95], v89 offset:32768
	ds_read_b128 v[96:99], v87 offset:49152
	s_waitcnt lgkmcnt(0)
	v_mfma_f32_32x32x16_f16 v[50:65], v[92:95], v[96:99], v[50:65]
	ds_read_b128 v[96:99], v87 offset:53248
	ds_read_b128 v[100:103], v87 offset:57344
	s_waitcnt lgkmcnt(0)
	v_mfma_f32_32x32x16_f16 v[34:49], v[92:95], v[96:99], v[34:49]
	v_mfma_f32_32x32x16_f16 v[18:33], v[92:95], v[100:103], v[18:33]
	ds_read_b128 v[96:99], v87 offset:61440
	ds_read_b128 v[100:103], v91 offset:32768
	s_waitcnt lgkmcnt(0)
	v_mfma_f32_32x32x16_f16 v[2:17], v[92:95], v[96:99], v[2:17]
	ds_read_b128 v[92:95], v90 offset:49152
	ds_read_b128 v[96:99], v90 offset:53248
	s_waitcnt lgkmcnt(0)
	v_mfma_f32_32x32x16_f16 v[50:65], v[100:103], v[92:95], v[50:65]
	v_mfma_f32_32x32x16_f16 v[34:49], v[100:103], v[96:99], v[34:49]
	ds_read_b128 v[92:95], v90 offset:57344
	ds_read_b128 v[96:99], v90 offset:61440
	s_waitcnt vmcnt(0) lgkmcnt(0)
	s_barrier
	v_mfma_f32_32x32x16_f16 v[18:33], v[100:103], v[92:95], v[18:33]
	v_lshl_add_u64 v[92:93], v[68:69], 0, s[20:21]
	global_load_lds_dwordx4 v[92:93], off
	v_lshl_add_u64 v[92:93], v[70:71], 0, s[20:21]
	s_mov_b32 m0, s2
	s_nop 0
	global_load_lds_dwordx4 v[92:93], off
	v_lshl_add_u64 v[92:93], v[72:73], 0, s[20:21]
	s_mov_b32 m0, s3
	v_mfma_f32_32x32x16_f16 v[2:17], v[100:103], v[96:99], v[2:17]
	global_load_lds_dwordx4 v[92:93], off
	v_lshl_add_u64 v[92:93], v[74:75], 0, s[20:21]
	s_mov_b32 m0, s4
	s_nop 0
	global_load_lds_dwordx4 v[92:93], off
	v_lshl_add_u64 v[92:93], v[76:77], 0, s[20:21]
	s_mov_b32 m0, s5
	s_nop 0
	global_load_lds_dwordx4 v[92:93], off
	v_lshl_add_u64 v[92:93], v[78:79], 0, s[20:21]
	s_mov_b32 m0, s6
	s_nop 0
	global_load_lds_dwordx4 v[92:93], off
	v_lshl_add_u64 v[92:93], v[80:81], 0, s[20:21]
	s_mov_b32 m0, s7
	s_nop 0
	global_load_lds_dwordx4 v[92:93], off
	v_lshl_add_u64 v[92:93], v[82:83], 0, s[20:21]
	s_mov_b32 m0, s8
	s_mov_b64 s[20:21], 0x200
	global_load_lds_dwordx4 v[92:93], off
	ds_read_b128 v[92:95], v86
	ds_read_b128 v[96:99], v85 offset:16384
	s_waitcnt lgkmcnt(0)
	v_mfma_f32_32x32x16_f16 v[50:65], v[92:95], v[96:99], v[50:65]
	ds_read_b128 v[96:99], v85 offset:20480
	ds_read_b128 v[100:103], v85 offset:24576
	s_mov_b32 m0, s9
	s_waitcnt lgkmcnt(0)
	v_mfma_f32_32x32x16_f16 v[34:49], v[92:95], v[96:99], v[34:49]
	v_mfma_f32_32x32x16_f16 v[18:33], v[92:95], v[100:103], v[18:33]
	ds_read_b128 v[96:99], v85 offset:28672
	ds_read_b128 v[100:103], v88
	s_waitcnt lgkmcnt(0)
	v_mfma_f32_32x32x16_f16 v[2:17], v[92:95], v[96:99], v[2:17]
	ds_read_b128 v[92:95], v0 offset:16384
	ds_read_b128 v[96:99], v0 offset:20480
	s_waitcnt lgkmcnt(0)
	v_mfma_f32_32x32x16_f16 v[50:65], v[100:103], v[92:95], v[50:65]
	v_mfma_f32_32x32x16_f16 v[34:49], v[100:103], v[96:99], v[34:49]
	ds_read_b128 v[92:95], v0 offset:24576
	ds_read_b128 v[96:99], v0 offset:28672
	s_waitcnt lgkmcnt(0)
	v_mfma_f32_32x32x16_f16 v[18:33], v[100:103], v[92:95], v[18:33]
	v_mfma_f32_32x32x16_f16 v[2:17], v[100:103], v[96:99], v[2:17]
	ds_read_b128 v[92:95], v89
	ds_read_b128 v[96:99], v87 offset:16384
	s_waitcnt lgkmcnt(0)
	v_mfma_f32_32x32x16_f16 v[50:65], v[92:95], v[96:99], v[50:65]
	ds_read_b128 v[96:99], v87 offset:20480
	ds_read_b128 v[100:103], v87 offset:24576
	s_waitcnt lgkmcnt(0)
	v_mfma_f32_32x32x16_f16 v[34:49], v[92:95], v[96:99], v[34:49]
	v_mfma_f32_32x32x16_f16 v[18:33], v[92:95], v[100:103], v[18:33]
	ds_read_b128 v[96:99], v87 offset:28672
	ds_read_b128 v[100:103], v91
	s_waitcnt lgkmcnt(0)
	v_mfma_f32_32x32x16_f16 v[2:17], v[92:95], v[96:99], v[2:17]
	ds_read_b128 v[92:95], v90 offset:16384
	ds_read_b128 v[96:99], v90 offset:20480
	s_waitcnt lgkmcnt(0)
	v_mfma_f32_32x32x16_f16 v[50:65], v[100:103], v[92:95], v[50:65]
	v_mfma_f32_32x32x16_f16 v[34:49], v[100:103], v[96:99], v[34:49]
	ds_read_b128 v[92:95], v90 offset:24576
	ds_read_b128 v[96:99], v90 offset:28672
	s_waitcnt vmcnt(0) lgkmcnt(0)
	s_barrier
	v_mfma_f32_32x32x16_f16 v[18:33], v[100:103], v[92:95], v[18:33]
	v_lshl_add_u64 v[92:93], v[68:69], 0, s[20:21]
	global_load_lds_dwordx4 v[92:93], off
	v_lshl_add_u64 v[92:93], v[70:71], 0, s[20:21]
	s_mov_b32 m0, s12
	s_nop 0
	global_load_lds_dwordx4 v[92:93], off
	v_lshl_add_u64 v[92:93], v[72:73], 0, s[20:21]
	s_mov_b32 m0, s13
	v_mfma_f32_32x32x16_f16 v[2:17], v[100:103], v[96:99], v[2:17]
	global_load_lds_dwordx4 v[92:93], off
	v_lshl_add_u64 v[92:93], v[74:75], 0, s[20:21]
	s_mov_b32 m0, s14
	s_nop 0
	global_load_lds_dwordx4 v[92:93], off
	v_lshl_add_u64 v[92:93], v[76:77], 0, s[20:21]
	s_mov_b32 m0, s15
	s_nop 0
	global_load_lds_dwordx4 v[92:93], off
	v_lshl_add_u64 v[92:93], v[78:79], 0, s[20:21]
	s_mov_b32 m0, s16
	s_nop 0
	global_load_lds_dwordx4 v[92:93], off
	v_lshl_add_u64 v[92:93], v[80:81], 0, s[20:21]
	s_mov_b32 m0, s17
	s_nop 0
	global_load_lds_dwordx4 v[92:93], off
	v_lshl_add_u64 v[92:93], v[82:83], 0, s[20:21]
	s_mov_b32 m0, s18
	s_mov_b64 s[20:21], 0x280
	global_load_lds_dwordx4 v[92:93], off
	ds_read_b128 v[92:95], v86 offset:32768
	ds_read_b128 v[96:99], v85 offset:49152
	s_waitcnt lgkmcnt(0)
	v_mfma_f32_32x32x16_f16 v[50:65], v[92:95], v[96:99], v[50:65]
	ds_read_b128 v[96:99], v85 offset:53248
	ds_read_b128 v[100:103], v85 offset:57344
	s_mov_b32 m0, s1
	s_waitcnt lgkmcnt(0)
	v_mfma_f32_32x32x16_f16 v[34:49], v[92:95], v[96:99], v[34:49]
	v_mfma_f32_32x32x16_f16 v[18:33], v[92:95], v[100:103], v[18:33]
	ds_read_b128 v[96:99], v85 offset:61440
	ds_read_b128 v[100:103], v88 offset:32768
	s_waitcnt lgkmcnt(0)
	v_mfma_f32_32x32x16_f16 v[2:17], v[92:95], v[96:99], v[2:17]
	ds_read_b128 v[92:95], v0 offset:49152
	ds_read_b128 v[96:99], v0 offset:53248
	s_waitcnt lgkmcnt(0)
	v_mfma_f32_32x32x16_f16 v[50:65], v[100:103], v[92:95], v[50:65]
	v_mfma_f32_32x32x16_f16 v[34:49], v[100:103], v[96:99], v[34:49]
	ds_read_b128 v[92:95], v0 offset:57344
	ds_read_b128 v[96:99], v0 offset:61440
	s_waitcnt lgkmcnt(0)
	v_mfma_f32_32x32x16_f16 v[18:33], v[100:103], v[92:95], v[18:33]
	v_mfma_f32_32x32x16_f16 v[2:17], v[100:103], v[96:99], v[2:17]
	ds_read_b128 v[92:95], v89 offset:32768
	ds_read_b128 v[96:99], v87 offset:49152
	s_waitcnt lgkmcnt(0)
	v_mfma_f32_32x32x16_f16 v[50:65], v[92:95], v[96:99], v[50:65]
	ds_read_b128 v[96:99], v87 offset:53248
	ds_read_b128 v[100:103], v87 offset:57344
	s_waitcnt lgkmcnt(0)
	v_mfma_f32_32x32x16_f16 v[34:49], v[92:95], v[96:99], v[34:49]
	v_mfma_f32_32x32x16_f16 v[18:33], v[92:95], v[100:103], v[18:33]
	ds_read_b128 v[96:99], v87 offset:61440
	ds_read_b128 v[100:103], v91 offset:32768
	s_waitcnt lgkmcnt(0)
	v_mfma_f32_32x32x16_f16 v[2:17], v[92:95], v[96:99], v[2:17]
	ds_read_b128 v[92:95], v90 offset:49152
	ds_read_b128 v[96:99], v90 offset:53248
	s_waitcnt lgkmcnt(0)
	v_mfma_f32_32x32x16_f16 v[50:65], v[100:103], v[92:95], v[50:65]
	v_mfma_f32_32x32x16_f16 v[34:49], v[100:103], v[96:99], v[34:49]
	ds_read_b128 v[92:95], v90 offset:57344
	ds_read_b128 v[96:99], v90 offset:61440
	s_waitcnt vmcnt(0) lgkmcnt(0)
	s_barrier
	v_mfma_f32_32x32x16_f16 v[18:33], v[100:103], v[92:95], v[18:33]
	v_lshl_add_u64 v[92:93], v[68:69], 0, s[20:21]
	global_load_lds_dwordx4 v[92:93], off
	v_lshl_add_u64 v[92:93], v[70:71], 0, s[20:21]
	s_mov_b32 m0, s2
	s_nop 0
	global_load_lds_dwordx4 v[92:93], off
	v_lshl_add_u64 v[92:93], v[72:73], 0, s[20:21]
	s_mov_b32 m0, s3
	v_mfma_f32_32x32x16_f16 v[2:17], v[100:103], v[96:99], v[2:17]
	global_load_lds_dwordx4 v[92:93], off
	v_lshl_add_u64 v[92:93], v[74:75], 0, s[20:21]
	s_mov_b32 m0, s4
	s_nop 0
	global_load_lds_dwordx4 v[92:93], off
	v_lshl_add_u64 v[92:93], v[76:77], 0, s[20:21]
	s_mov_b32 m0, s5
	s_nop 0
	global_load_lds_dwordx4 v[92:93], off
	v_lshl_add_u64 v[92:93], v[78:79], 0, s[20:21]
	s_mov_b32 m0, s6
	s_nop 0
	global_load_lds_dwordx4 v[92:93], off
	v_lshl_add_u64 v[92:93], v[80:81], 0, s[20:21]
	s_mov_b32 m0, s7
	s_nop 0
	global_load_lds_dwordx4 v[92:93], off
	v_lshl_add_u64 v[92:93], v[82:83], 0, s[20:21]
	s_mov_b32 m0, s8
	s_mov_b64 s[20:21], 0x300
	global_load_lds_dwordx4 v[92:93], off
	ds_read_b128 v[92:95], v86
	ds_read_b128 v[96:99], v85 offset:16384
	s_waitcnt lgkmcnt(0)
	v_mfma_f32_32x32x16_f16 v[50:65], v[92:95], v[96:99], v[50:65]
	ds_read_b128 v[96:99], v85 offset:20480
	ds_read_b128 v[100:103], v85 offset:24576
	s_mov_b32 m0, s9
	s_waitcnt lgkmcnt(0)
	v_mfma_f32_32x32x16_f16 v[34:49], v[92:95], v[96:99], v[34:49]
	v_mfma_f32_32x32x16_f16 v[18:33], v[92:95], v[100:103], v[18:33]
	ds_read_b128 v[96:99], v85 offset:28672
	ds_read_b128 v[100:103], v88
	s_waitcnt lgkmcnt(0)
	v_mfma_f32_32x32x16_f16 v[2:17], v[92:95], v[96:99], v[2:17]
	ds_read_b128 v[92:95], v0 offset:16384
	ds_read_b128 v[96:99], v0 offset:20480
	s_waitcnt lgkmcnt(0)
	v_mfma_f32_32x32x16_f16 v[50:65], v[100:103], v[92:95], v[50:65]
	v_mfma_f32_32x32x16_f16 v[34:49], v[100:103], v[96:99], v[34:49]
	ds_read_b128 v[92:95], v0 offset:24576
	ds_read_b128 v[96:99], v0 offset:28672
	s_waitcnt lgkmcnt(0)
	v_mfma_f32_32x32x16_f16 v[18:33], v[100:103], v[92:95], v[18:33]
	v_mfma_f32_32x32x16_f16 v[2:17], v[100:103], v[96:99], v[2:17]
	ds_read_b128 v[92:95], v89
	ds_read_b128 v[96:99], v87 offset:16384
	s_waitcnt lgkmcnt(0)
	v_mfma_f32_32x32x16_f16 v[50:65], v[92:95], v[96:99], v[50:65]
	ds_read_b128 v[96:99], v87 offset:20480
	ds_read_b128 v[100:103], v87 offset:24576
	s_waitcnt lgkmcnt(0)
	v_mfma_f32_32x32x16_f16 v[34:49], v[92:95], v[96:99], v[34:49]
	v_mfma_f32_32x32x16_f16 v[18:33], v[92:95], v[100:103], v[18:33]
	ds_read_b128 v[96:99], v87 offset:28672
	ds_read_b128 v[100:103], v91
	s_waitcnt lgkmcnt(0)
	v_mfma_f32_32x32x16_f16 v[2:17], v[92:95], v[96:99], v[2:17]
	ds_read_b128 v[92:95], v90 offset:16384
	ds_read_b128 v[96:99], v90 offset:20480
	s_waitcnt lgkmcnt(0)
	v_mfma_f32_32x32x16_f16 v[50:65], v[100:103], v[92:95], v[50:65]
	v_mfma_f32_32x32x16_f16 v[34:49], v[100:103], v[96:99], v[34:49]
	ds_read_b128 v[92:95], v90 offset:24576
	ds_read_b128 v[96:99], v90 offset:28672
	s_waitcnt vmcnt(0) lgkmcnt(0)
	s_barrier
	v_mfma_f32_32x32x16_f16 v[18:33], v[100:103], v[92:95], v[18:33]
	v_lshl_add_u64 v[92:93], v[68:69], 0, s[20:21]
	global_load_lds_dwordx4 v[92:93], off
	v_lshl_add_u64 v[92:93], v[70:71], 0, s[20:21]
	s_mov_b32 m0, s12
	s_nop 0
	global_load_lds_dwordx4 v[92:93], off
	v_lshl_add_u64 v[92:93], v[72:73], 0, s[20:21]
	s_mov_b32 m0, s13
	v_mfma_f32_32x32x16_f16 v[2:17], v[100:103], v[96:99], v[2:17]
	global_load_lds_dwordx4 v[92:93], off
	v_lshl_add_u64 v[92:93], v[74:75], 0, s[20:21]
	s_mov_b32 m0, s14
	s_mov_b64 s[12:13], 0x380
	global_load_lds_dwordx4 v[92:93], off
	v_lshl_add_u64 v[92:93], v[76:77], 0, s[20:21]
	s_mov_b32 m0, s15
	v_lshl_add_u64 v[68:69], v[68:69], 0, s[12:13]
	global_load_lds_dwordx4 v[92:93], off
	v_lshl_add_u64 v[92:93], v[78:79], 0, s[20:21]
	s_mov_b32 m0, s16
	s_nop 0
	global_load_lds_dwordx4 v[92:93], off
	v_lshl_add_u64 v[92:93], v[80:81], 0, s[20:21]
	s_mov_b32 m0, s17
	s_nop 0
	global_load_lds_dwordx4 v[92:93], off
	v_lshl_add_u64 v[92:93], v[82:83], 0, s[20:21]
	s_mov_b32 m0, s18
	s_nop 0
	global_load_lds_dwordx4 v[92:93], off
	ds_read_b128 v[92:95], v86 offset:32768
	ds_read_b128 v[96:99], v85 offset:49152
	s_waitcnt lgkmcnt(0)
	v_mfma_f32_32x32x16_f16 v[50:65], v[92:95], v[96:99], v[50:65]
	ds_read_b128 v[96:99], v85 offset:53248
	ds_read_b128 v[100:103], v85 offset:57344
	s_mov_b32 m0, s1
	s_waitcnt lgkmcnt(0)
	v_mfma_f32_32x32x16_f16 v[34:49], v[92:95], v[96:99], v[34:49]
	v_mfma_f32_32x32x16_f16 v[18:33], v[92:95], v[100:103], v[18:33]
	ds_read_b128 v[96:99], v85 offset:61440
	ds_read_b128 v[100:103], v88 offset:32768
	s_waitcnt lgkmcnt(0)
	v_mfma_f32_32x32x16_f16 v[2:17], v[92:95], v[96:99], v[2:17]
	ds_read_b128 v[92:95], v0 offset:49152
	ds_read_b128 v[96:99], v0 offset:53248
	s_waitcnt lgkmcnt(0)
	v_mfma_f32_32x32x16_f16 v[50:65], v[100:103], v[92:95], v[50:65]
	v_mfma_f32_32x32x16_f16 v[34:49], v[100:103], v[96:99], v[34:49]
	ds_read_b128 v[92:95], v0 offset:57344
	ds_read_b128 v[96:99], v0 offset:61440
	s_waitcnt lgkmcnt(0)
	v_mfma_f32_32x32x16_f16 v[18:33], v[100:103], v[92:95], v[18:33]
	v_mfma_f32_32x32x16_f16 v[2:17], v[100:103], v[96:99], v[2:17]
	ds_read_b128 v[92:95], v89 offset:32768
	ds_read_b128 v[96:99], v87 offset:49152
	s_waitcnt lgkmcnt(0)
	v_mfma_f32_32x32x16_f16 v[50:65], v[92:95], v[96:99], v[50:65]
	ds_read_b128 v[96:99], v87 offset:53248
	ds_read_b128 v[100:103], v87 offset:57344
	s_waitcnt lgkmcnt(0)
	v_mfma_f32_32x32x16_f16 v[34:49], v[92:95], v[96:99], v[34:49]
	v_mfma_f32_32x32x16_f16 v[18:33], v[92:95], v[100:103], v[18:33]
	ds_read_b128 v[96:99], v87 offset:61440
	ds_read_b128 v[100:103], v91 offset:32768
	s_waitcnt lgkmcnt(0)
	v_mfma_f32_32x32x16_f16 v[2:17], v[92:95], v[96:99], v[2:17]
	ds_read_b128 v[92:95], v90 offset:49152
	ds_read_b128 v[96:99], v90 offset:53248
	s_waitcnt lgkmcnt(0)
	v_mfma_f32_32x32x16_f16 v[50:65], v[100:103], v[92:95], v[50:65]
	v_mfma_f32_32x32x16_f16 v[34:49], v[100:103], v[96:99], v[34:49]
	ds_read_b128 v[92:95], v90 offset:57344
	ds_read_b128 v[96:99], v90 offset:61440
	s_waitcnt vmcnt(0) lgkmcnt(0)
	s_barrier
	global_load_lds_dwordx4 v[68:69], off
	v_lshl_add_u64 v[68:69], v[70:71], 0, s[12:13]
	s_mov_b32 m0, s2
	v_mfma_f32_32x32x16_f16 v[18:33], v[100:103], v[92:95], v[18:33]
	global_load_lds_dwordx4 v[68:69], off
	v_lshl_add_u64 v[68:69], v[72:73], 0, s[12:13]
	s_mov_b32 m0, s3
	s_cselect_b64 s[2:3], -1, 0
	global_load_lds_dwordx4 v[68:69], off
	v_lshl_add_u64 v[68:69], v[74:75], 0, s[12:13]
	s_mov_b32 m0, s4
	v_mfma_f32_32x32x16_f16 v[2:17], v[100:103], v[96:99], v[2:17]
	global_load_lds_dwordx4 v[68:69], off
	v_lshl_add_u64 v[68:69], v[76:77], 0, s[12:13]
	s_mov_b32 m0, s5
	s_cmpk_lt_u32 s0, 0x2a99
	global_load_lds_dwordx4 v[68:69], off
	v_lshl_add_u64 v[68:69], v[78:79], 0, s[12:13]
	s_mov_b32 m0, s6
	s_nop 0
	global_load_lds_dwordx4 v[68:69], off
	v_lshl_add_u64 v[68:69], v[80:81], 0, s[12:13]
	s_mov_b32 m0, s7
	s_nop 0
	global_load_lds_dwordx4 v[68:69], off
	v_lshl_add_u64 v[68:69], v[82:83], 0, s[12:13]
	s_mov_b32 m0, s8
	s_nop 0
	global_load_lds_dwordx4 v[68:69], off
	ds_read_b128 v[68:71], v86
	ds_read_b128 v[72:75], v85 offset:16384
	s_waitcnt lgkmcnt(0)
	v_mfma_f32_32x32x16_f16 v[50:65], v[68:71], v[72:75], v[50:65]
	ds_read_b128 v[72:75], v85 offset:20480
	ds_read_b128 v[76:79], v85 offset:24576
	s_waitcnt lgkmcnt(0)
	v_mfma_f32_32x32x16_f16 v[34:49], v[68:71], v[72:75], v[34:49]
	v_mfma_f32_32x32x16_f16 v[18:33], v[68:71], v[76:79], v[18:33]
	ds_read_b128 v[72:75], v85 offset:28672
	ds_read_b128 v[76:79], v88
	s_waitcnt lgkmcnt(0)
	v_mfma_f32_32x32x16_f16 v[2:17], v[68:71], v[72:75], v[2:17]
	ds_read_b128 v[68:71], v0 offset:16384
	ds_read_b128 v[72:75], v0 offset:20480
	s_waitcnt lgkmcnt(0)
	v_mfma_f32_32x32x16_f16 v[50:65], v[76:79], v[68:71], v[50:65]
	v_mfma_f32_32x32x16_f16 v[34:49], v[76:79], v[72:75], v[34:49]
	ds_read_b128 v[68:71], v0 offset:24576
	ds_read_b128 v[72:75], v0 offset:28672
	s_waitcnt lgkmcnt(0)
	v_mfma_f32_32x32x16_f16 v[18:33], v[76:79], v[68:71], v[18:33]
	v_mfma_f32_32x32x16_f16 v[2:17], v[76:79], v[72:75], v[2:17]
	ds_read_b128 v[68:71], v89
	ds_read_b128 v[72:75], v87 offset:16384
	s_waitcnt lgkmcnt(0)
	v_mfma_f32_32x32x16_f16 v[50:65], v[68:71], v[72:75], v[50:65]
	ds_read_b128 v[72:75], v87 offset:20480
	ds_read_b128 v[76:79], v87 offset:24576
	s_waitcnt lgkmcnt(0)
	v_mfma_f32_32x32x16_f16 v[34:49], v[68:71], v[72:75], v[34:49]
	v_mfma_f32_32x32x16_f16 v[18:33], v[68:71], v[76:79], v[18:33]
	ds_read_b128 v[72:75], v87 offset:28672
	ds_read_b128 v[76:79], v91
	s_waitcnt lgkmcnt(0)
	v_mfma_f32_32x32x16_f16 v[2:17], v[68:71], v[72:75], v[2:17]
	ds_read_b128 v[68:71], v90 offset:16384
	ds_read_b128 v[72:75], v90 offset:20480
	s_waitcnt lgkmcnt(0)
	v_mfma_f32_32x32x16_f16 v[50:65], v[76:79], v[68:71], v[50:65]
	v_mfma_f32_32x32x16_f16 v[34:49], v[76:79], v[72:75], v[34:49]
	ds_read_b128 v[68:71], v90 offset:24576
	ds_read_b128 v[72:75], v90 offset:28672
	s_waitcnt vmcnt(0) lgkmcnt(0)
	s_barrier
	v_mfma_f32_32x32x16_f16 v[18:33], v[76:79], v[68:71], v[18:33]
	v_mfma_f32_32x32x16_f16 v[2:17], v[76:79], v[72:75], v[2:17]
	ds_read_b128 v[68:71], v86 offset:32768
	ds_read_b128 v[72:75], v85 offset:49152
	s_waitcnt lgkmcnt(0)
	v_mfma_f32_32x32x16_f16 v[50:65], v[68:71], v[72:75], v[50:65]
	ds_read_b128 v[72:75], v85 offset:53248
	s_waitcnt lgkmcnt(0)
	v_mfma_f32_32x32x16_f16 v[34:49], v[68:71], v[72:75], v[34:49]
	ds_read_b128 v[72:75], v85 offset:57344
	s_waitcnt lgkmcnt(0)
	v_mfma_f32_32x32x16_f16 v[18:33], v[68:71], v[72:75], v[18:33]
	ds_read_b128 v[72:75], v85 offset:61440
	s_waitcnt lgkmcnt(0)
	v_mfma_f32_32x32x16_f16 v[2:17], v[68:71], v[72:75], v[2:17]
	ds_read_b128 v[68:71], v88 offset:32768
	ds_read_b128 v[72:75], v0 offset:49152
	s_waitcnt lgkmcnt(0)
	v_mfma_f32_32x32x16_f16 v[50:65], v[68:71], v[72:75], v[50:65]
	ds_read_b128 v[72:75], v0 offset:53248
	s_waitcnt lgkmcnt(0)
	v_mfma_f32_32x32x16_f16 v[34:49], v[68:71], v[72:75], v[34:49]
	ds_read_b128 v[72:75], v0 offset:57344
	s_waitcnt lgkmcnt(0)
	v_mfma_f32_32x32x16_f16 v[18:33], v[68:71], v[72:75], v[18:33]
	ds_read_b128 v[72:75], v0 offset:61440
	s_waitcnt lgkmcnt(0)
	v_mfma_f32_32x32x16_f16 v[2:17], v[68:71], v[72:75], v[2:17]
	ds_read_b128 v[68:71], v89 offset:32768
	ds_read_b128 v[72:75], v87 offset:49152
	s_waitcnt lgkmcnt(0)
	v_mfma_f32_32x32x16_f16 v[50:65], v[68:71], v[72:75], v[50:65]
	ds_read_b128 v[72:75], v87 offset:53248
	s_waitcnt lgkmcnt(0)
	v_mfma_f32_32x32x16_f16 v[34:49], v[68:71], v[72:75], v[34:49]
	ds_read_b128 v[72:75], v87 offset:57344
	s_waitcnt lgkmcnt(0)
	v_mfma_f32_32x32x16_f16 v[18:33], v[68:71], v[72:75], v[18:33]
	ds_read_b128 v[72:75], v87 offset:61440
	s_waitcnt lgkmcnt(0)
	v_mfma_f32_32x32x16_f16 v[2:17], v[68:71], v[72:75], v[2:17]
	ds_read_b128 v[70:73], v91 offset:32768
	ds_read_b128 v[74:77], v90 offset:49152
	v_or_b32_e32 v68, s0, v1
	v_lshl_or_b32 v0, v84, 2, v68
	v_mov_b32_e32 v1, v67
	v_lshlrev_b64 v[0:1], 11, v[0:1]
	v_lshl_add_u64 v[0:1], s[10:11], 0, v[0:1]
	v_lshl_add_u64 v[0:1], v[0:1], 0, v[66:67]
	s_waitcnt lgkmcnt(0)
	v_mfma_f32_32x32x16_f16 v[50:65], v[70:73], v[74:77], v[50:65]
	ds_read_b128 v[74:77], v90 offset:53248
	s_mov_b64 s[0:1], -1
	s_waitcnt lgkmcnt(0)
	v_mfma_f32_32x32x16_f16 v[34:49], v[70:73], v[74:77], v[34:49]
	ds_read_b128 v[74:77], v90 offset:61440
	ds_read_b128 v[78:81], v90 offset:57344
	s_waitcnt lgkmcnt(0)
	s_barrier
	v_mfma_f32_32x32x16_f16 v[18:33], v[70:73], v[78:81], v[18:33]
	v_mfma_f32_32x32x16_f16 v[2:17], v[70:73], v[74:77], v[2:17]
	s_cbranch_scc1 .LBB4_10
	s_movk_i32 s4, 0x2b18
	v_cmp_gt_u32_e32 vcc, s4, v68
	s_and_saveexec_b64 s[0:1], vcc
	s_cbranch_execz .LBB4_3
	v_add_co_u32_e32 v66, vcc, 0x1000, v0
	global_store_dword v[0:1], v50, off nt
	global_store_dword v[0:1], v51, off offset:2048 nt
	v_addc_co_u32_e32 v67, vcc, 0, v1, vcc
	global_store_dword v[66:67], v52, off nt
	global_store_dword v[66:67], v53, off offset:2048 nt
